# t9_Bplus_nt_rev
# speedup vs baseline: 1.0238x; 1.0238x over previous
_Z11align_fusedPKfS0_PKiPf:
	s_load_dwordx8 s[4:11], s[0:1], 0x0
	s_sub_u32 s2, 0x1fff, s2
	s_mul_i32 s12, s2, 0x5dc0
	v_and_b32_e32 v7, 63, v0
	v_readfirstlane_b32 s13, v0
	v_lshlrev_b32_e32 v1, 4, v7
	v_mul_u32_u24_e32 v3, 12, v7
	s_mul_i32 s18, s13, 96
	s_mul_i32 s3, s13, 6
	s_sub_u32 s3, 0x49c, s3
	v_cmp_gt_u32_e64 s[14:15], s3, v7
	v_add_u32_e32 v2, s18, v1
	v_add_u32_e32 v3, s18, v3
	v_add_u32_e32 v4, 0x600, v3
	s_add_u32 s12, s12, s18
	s_add_u32 s12, s12, 0x800
	s_waitcnt lgkmcnt(0)
	s_add_u32 s4, s4, s12
	s_addc_u32 s5, s5, 0
	s_add_u32 s10, s10, s12
	s_addc_u32 s11, s11, 0
	s_cmp_lg_u32 s13, 0
	s_cbranch_scc1 .Lbulk_waves
	v_lshlrev_b32_e32 v5, 2, v7
	global_load_dword v5, v5, s[8:9]
	global_load_dwordx3 v[44:46], v3, s[6:7] nt
	global_load_dwordx4 v[8:11], v1, s[4:5] offset:-2048 nt
	global_load_dwordx4 v[12:15], v1, s[4:5] offset:-1024 nt
	global_load_dwordx4 v[16:19], v1, s[4:5] offset:0 nt
	global_load_dwordx4 v[20:23], v1, s[4:5] offset:1024 nt
	global_load_dwordx4 v[24:27], v1, s[4:5] offset:2048 nt
	global_load_dwordx4 v[28:31], v1, s[4:5] offset:3072 nt
	s_mov_b32 s20, 0
	s_mov_b32 s21, 0x10000
	s_mov_b32 s22, 0
	s_mov_b32 s23, 0x20000
	s_mov_b32 s24, 0
	s_mov_b32 s25, 0x40000
	s_mov_b32 s26, 0
	s_mov_b32 s27, 0x80000
	s_waitcnt vmcnt(6)
	v_mul_u32_u24_e32 v5, 12, v5
	v_add_f32_dpp v52, v44, v44 quad_perm:[1,0,3,2] row_mask:0xf bank_mask:0xf
	v_add_f32_dpp v53, v45, v45 quad_perm:[1,0,3,2] row_mask:0xf bank_mask:0xf
	v_add_f32_dpp v54, v46, v46 quad_perm:[1,0,3,2] row_mask:0xf bank_mask:0xf
	v_add_f32_dpp v52, v52, v52 quad_perm:[2,3,0,1] row_mask:0xf bank_mask:0xf
	v_add_f32_dpp v53, v53, v53 quad_perm:[2,3,0,1] row_mask:0xf bank_mask:0xf
	v_add_f32_dpp v54, v54, v54 quad_perm:[2,3,0,1] row_mask:0xf bank_mask:0xf
	v_add_f32_dpp v52, v52, v52 row_half_mirror row_mask:0xf bank_mask:0xf
	v_add_f32_dpp v53, v53, v53 row_half_mirror row_mask:0xf bank_mask:0xf
	v_add_f32_dpp v54, v54, v54 row_half_mirror row_mask:0xf bank_mask:0xf
	v_add_f32_dpp v52, v52, v52 row_mirror row_mask:0xf bank_mask:0xf
	v_add_f32_dpp v53, v53, v53 row_mirror row_mask:0xf bank_mask:0xf
	v_add_f32_dpp v54, v54, v54 row_mirror row_mask:0xf bank_mask:0xf
	v_add_f32_dpp v52, v52, v52 row_bcast:15 row_mask:0xa bank_mask:0xf
	v_add_f32_dpp v53, v53, v53 row_bcast:15 row_mask:0xa bank_mask:0xf
	v_add_f32_dpp v54, v54, v54 row_bcast:15 row_mask:0xa bank_mask:0xf
	v_add_f32_dpp v52, v52, v52 row_bcast:31 row_mask:0xc bank_mask:0xf
	v_add_f32_dpp v53, v53, v53 row_bcast:31 row_mask:0xc bank_mask:0xf
	v_add_f32_dpp v54, v54, v54 row_bcast:31 row_mask:0xc bank_mask:0xf
	v_readlane_b32 s28, v52, 63
	v_readlane_b32 s29, v53, 63
	v_readlane_b32 s30, v54, 63
	v_mov_b32_e32 v52, s28
	v_mov_b32_e32 v53, s29
	v_mov_b32_e32 v54, s30
	v_fmac_f32_e32 v44, 0xbc800000, v52
	v_fmac_f32_e32 v45, 0xbc800000, v53
	v_fmac_f32_e32 v46, 0xbc800000, v54
	s_waitcnt vmcnt(0)
	ds_write_b128 v2, v[8:11]
	ds_write_b128 v2, v[12:15] offset:1024
	ds_write_b128 v2, v[16:19] offset:2048
	ds_write_b128 v2, v[20:23] offset:3072
	ds_write_b128 v2, v[24:27] offset:4096
	ds_write_b128 v2, v[28:31] offset:5120
	s_waitcnt lgkmcnt(0)
	s_barrier
	ds_read_b32 v48, v5
	ds_read_b32 v49, v5 offset:4
	ds_read_b32 v50, v5 offset:8
	s_waitcnt lgkmcnt(0)
	v_add_f32_dpp v52, v48, v48 quad_perm:[1,0,3,2] row_mask:0xf bank_mask:0xf
	v_add_f32_dpp v53, v49, v49 quad_perm:[1,0,3,2] row_mask:0xf bank_mask:0xf
	v_add_f32_dpp v54, v50, v50 quad_perm:[1,0,3,2] row_mask:0xf bank_mask:0xf
	v_add_f32_dpp v52, v52, v52 quad_perm:[2,3,0,1] row_mask:0xf bank_mask:0xf
	v_add_f32_dpp v53, v53, v53 quad_perm:[2,3,0,1] row_mask:0xf bank_mask:0xf
	v_add_f32_dpp v54, v54, v54 quad_perm:[2,3,0,1] row_mask:0xf bank_mask:0xf
	v_add_f32_dpp v52, v52, v52 row_half_mirror row_mask:0xf bank_mask:0xf
	v_add_f32_dpp v53, v53, v53 row_half_mirror row_mask:0xf bank_mask:0xf
	v_add_f32_dpp v54, v54, v54 row_half_mirror row_mask:0xf bank_mask:0xf
	v_add_f32_dpp v52, v52, v52 row_mirror row_mask:0xf bank_mask:0xf
	v_add_f32_dpp v53, v53, v53 row_mirror row_mask:0xf bank_mask:0xf
	v_add_f32_dpp v54, v54, v54 row_mirror row_mask:0xf bank_mask:0xf
	v_add_f32_dpp v52, v52, v52 row_bcast:15 row_mask:0xa bank_mask:0xf
	v_add_f32_dpp v53, v53, v53 row_bcast:15 row_mask:0xa bank_mask:0xf
	v_add_f32_dpp v54, v54, v54 row_bcast:15 row_mask:0xa bank_mask:0xf
	v_add_f32_dpp v52, v52, v52 row_bcast:31 row_mask:0xc bank_mask:0xf
	v_add_f32_dpp v53, v53, v53 row_bcast:31 row_mask:0xc bank_mask:0xf
	v_add_f32_dpp v54, v54, v54 row_bcast:31 row_mask:0xc bank_mask:0xf
	v_readlane_b32 s32, v52, 63
	v_readlane_b32 s33, v53, 63
	v_readlane_b32 s34, v54, 63
	v_mov_b32_e32 v52, s32
	v_mov_b32_e32 v53, s33
	v_mov_b32_e32 v54, s34
	v_fmac_f32_e32 v48, 0xbc800000, v52
	v_fmac_f32_e32 v49, 0xbc800000, v53
	v_fmac_f32_e32 v50, 0xbc800000, v54
	v_mul_f32_e32 v52, v48, v44
	v_mul_f32_e32 v53, v48, v45
	v_mul_f32_e32 v54, v48, v46
	v_mul_f32_e32 v55, v49, v44
	v_mul_f32_e32 v56, v49, v45
	v_mul_f32_e32 v57, v49, v46
	v_mul_f32_e32 v58, v50, v44
	v_mul_f32_e32 v59, v50, v45
	v_mul_f32_e32 v60, v50, v46
	v_add_f32_dpp v52, v52, v52 quad_perm:[1,0,3,2] row_mask:0xf bank_mask:0xf
	v_add_f32_dpp v53, v53, v53 quad_perm:[1,0,3,2] row_mask:0xf bank_mask:0xf
	v_add_f32_dpp v54, v54, v54 quad_perm:[1,0,3,2] row_mask:0xf bank_mask:0xf
	v_add_f32_dpp v55, v55, v55 quad_perm:[1,0,3,2] row_mask:0xf bank_mask:0xf
	v_add_f32_dpp v56, v56, v56 quad_perm:[1,0,3,2] row_mask:0xf bank_mask:0xf
	v_add_f32_dpp v57, v57, v57 quad_perm:[1,0,3,2] row_mask:0xf bank_mask:0xf
	v_add_f32_dpp v58, v58, v58 quad_perm:[1,0,3,2] row_mask:0xf bank_mask:0xf
	v_add_f32_dpp v59, v59, v59 quad_perm:[1,0,3,2] row_mask:0xf bank_mask:0xf
	v_add_f32_dpp v60, v60, v60 quad_perm:[1,0,3,2] row_mask:0xf bank_mask:0xf
	v_add_f32_dpp v52, v52, v52 quad_perm:[2,3,0,1] row_mask:0xf bank_mask:0xf
	v_add_f32_dpp v53, v53, v53 quad_perm:[2,3,0,1] row_mask:0xf bank_mask:0xf
	v_add_f32_dpp v54, v54, v54 quad_perm:[2,3,0,1] row_mask:0xf bank_mask:0xf
	v_add_f32_dpp v55, v55, v55 quad_perm:[2,3,0,1] row_mask:0xf bank_mask:0xf
	v_add_f32_dpp v56, v56, v56 quad_perm:[2,3,0,1] row_mask:0xf bank_mask:0xf
	v_add_f32_dpp v57, v57, v57 quad_perm:[2,3,0,1] row_mask:0xf bank_mask:0xf
	v_add_f32_dpp v58, v58, v58 quad_perm:[2,3,0,1] row_mask:0xf bank_mask:0xf
	v_add_f32_dpp v59, v59, v59 quad_perm:[2,3,0,1] row_mask:0xf bank_mask:0xf
	v_add_f32_dpp v60, v60, v60 quad_perm:[2,3,0,1] row_mask:0xf bank_mask:0xf
	v_add_f32_dpp v52, v52, v52 row_half_mirror row_mask:0xf bank_mask:0xf
	v_add_f32_dpp v53, v53, v53 row_half_mirror row_mask:0xf bank_mask:0xf
	v_add_f32_dpp v54, v54, v54 row_half_mirror row_mask:0xf bank_mask:0xf
	v_add_f32_dpp v55, v55, v55 row_half_mirror row_mask:0xf bank_mask:0xf
	v_add_f32_dpp v56, v56, v56 row_half_mirror row_mask:0xf bank_mask:0xf
	v_add_f32_dpp v57, v57, v57 row_half_mirror row_mask:0xf bank_mask:0xf
	v_add_f32_dpp v58, v58, v58 row_half_mirror row_mask:0xf bank_mask:0xf
	v_add_f32_dpp v59, v59, v59 row_half_mirror row_mask:0xf bank_mask:0xf
	v_add_f32_dpp v60, v60, v60 row_half_mirror row_mask:0xf bank_mask:0xf
	v_add_f32_dpp v52, v52, v52 row_mirror row_mask:0xf bank_mask:0xf
	v_add_f32_dpp v53, v53, v53 row_mirror row_mask:0xf bank_mask:0xf
	v_add_f32_dpp v54, v54, v54 row_mirror row_mask:0xf bank_mask:0xf
	v_add_f32_dpp v55, v55, v55 row_mirror row_mask:0xf bank_mask:0xf
	v_add_f32_dpp v56, v56, v56 row_mirror row_mask:0xf bank_mask:0xf
	v_add_f32_dpp v57, v57, v57 row_mirror row_mask:0xf bank_mask:0xf
	v_add_f32_dpp v58, v58, v58 row_mirror row_mask:0xf bank_mask:0xf
	v_add_f32_dpp v59, v59, v59 row_mirror row_mask:0xf bank_mask:0xf
	v_add_f32_dpp v60, v60, v60 row_mirror row_mask:0xf bank_mask:0xf
	v_add_f32_dpp v52, v52, v52 row_bcast:15 row_mask:0xa bank_mask:0xf
	v_add_f32_dpp v53, v53, v53 row_bcast:15 row_mask:0xa bank_mask:0xf
	v_add_f32_dpp v54, v54, v54 row_bcast:15 row_mask:0xa bank_mask:0xf
	v_add_f32_dpp v55, v55, v55 row_bcast:15 row_mask:0xa bank_mask:0xf
	v_add_f32_dpp v56, v56, v56 row_bcast:15 row_mask:0xa bank_mask:0xf
	v_add_f32_dpp v57, v57, v57 row_bcast:15 row_mask:0xa bank_mask:0xf
	v_add_f32_dpp v58, v58, v58 row_bcast:15 row_mask:0xa bank_mask:0xf
	v_add_f32_dpp v59, v59, v59 row_bcast:15 row_mask:0xa bank_mask:0xf
	v_add_f32_dpp v60, v60, v60 row_bcast:15 row_mask:0xa bank_mask:0xf
	v_add_f32_dpp v52, v52, v52 row_bcast:31 row_mask:0xc bank_mask:0xf
	v_add_f32_dpp v53, v53, v53 row_bcast:31 row_mask:0xc bank_mask:0xf
	v_add_f32_dpp v54, v54, v54 row_bcast:31 row_mask:0xc bank_mask:0xf
	v_add_f32_dpp v55, v55, v55 row_bcast:31 row_mask:0xc bank_mask:0xf
	v_add_f32_dpp v56, v56, v56 row_bcast:31 row_mask:0xc bank_mask:0xf
	v_add_f32_dpp v57, v57, v57 row_bcast:31 row_mask:0xc bank_mask:0xf
	v_add_f32_dpp v58, v58, v58 row_bcast:31 row_mask:0xc bank_mask:0xf
	v_add_f32_dpp v59, v59, v59 row_bcast:31 row_mask:0xc bank_mask:0xf
	v_add_f32_dpp v60, v60, v60 row_bcast:31 row_mask:0xc bank_mask:0xf
	v_cndmask_b32_e64 v52, v52, v55, s[22:23]
	v_cndmask_b32_e64 v53, v53, v56, s[22:23]
	v_cndmask_b32_e64 v54, v54, v57, s[22:23]
	v_cndmask_b32_e64 v52, v52, v58, s[24:25]
	v_cndmask_b32_e64 v53, v53, v59, s[24:25]
	v_cndmask_b32_e64 v54, v54, v60, s[24:25]
	v_cndmask_b32_e64 v52, v52, 0, s[26:27]
	v_cndmask_b32_e64 v53, v53, 0, s[26:27]
	v_cndmask_b32_e64 v54, v54, 0, s[26:27]
	v_cndmask_b32_e64 v40, 0, 1.0, s[20:21]
	v_cndmask_b32_e64 v41, 0, 1.0, s[22:23]
	v_cndmask_b32_e64 v42, 0, 1.0, s[24:25]
	v_mul_f32_e32 v55, v52, v52
	v_mul_f32_e32 v56, v53, v53
	v_mul_f32_e32 v57, v52, v53
	v_add_f32_dpp v55, v55, v55 quad_perm:[1,0,3,2] row_mask:0xf bank_mask:0xf
	v_add_f32_dpp v56, v56, v56 quad_perm:[1,0,3,2] row_mask:0xf bank_mask:0xf
	v_add_f32_dpp v57, v57, v57 quad_perm:[1,0,3,2] row_mask:0xf bank_mask:0xf
	v_add_f32_dpp v55, v55, v55 quad_perm:[2,3,0,1] row_mask:0xf bank_mask:0xf
	v_add_f32_dpp v56, v56, v56 quad_perm:[2,3,0,1] row_mask:0xf bank_mask:0xf
	v_add_f32_dpp v57, v57, v57 quad_perm:[2,3,0,1] row_mask:0xf bank_mask:0xf
	v_sub_f32_e32 v60, v56, v55
	v_mul_f32_e32 v58, v57, v57
	v_cmp_gt_f32_e32 vcc, 0, v60
	v_mul_f32_e32 v59, v60, v60
	v_fmac_f32_e32 v59, 4.0, v58
	v_sqrt_f32_e32 v59, v59
	s_nop 0
	v_add_f32_e64 v59, |v60|, v59
	v_add_f32_e32 v59, 0x0da24260, v59
	v_rcp_f32_e32 v59, v59
	v_add_f32_e32 v58, v57, v57
	v_mul_f32_e32 v59, v58, v59
	v_cndmask_b32_e64 v59, v59, -v59, vcc
	v_fma_f32 v58, v59, v59, 1.0
	v_rsq_f32_e32 v61, v58
	s_nop 0
	v_mul_f32_e32 v62, v61, v59
	v_mul_f32_e32 v55, v62, v53
	v_mul_f32_e32 v56, v62, v52
	v_fma_f32 v52, v61, v52, -v55
	v_fma_f32 v53, v61, v53, v56
	v_mul_f32_e32 v55, v52, v52
	v_mul_f32_e32 v56, v54, v54
	v_mul_f32_e32 v57, v52, v54
	v_add_f32_dpp v55, v55, v55 quad_perm:[1,0,3,2] row_mask:0xf bank_mask:0xf
	v_add_f32_dpp v56, v56, v56 quad_perm:[1,0,3,2] row_mask:0xf bank_mask:0xf
	v_add_f32_dpp v57, v57, v57 quad_perm:[1,0,3,2] row_mask:0xf bank_mask:0xf
	v_add_f32_dpp v55, v55, v55 quad_perm:[2,3,0,1] row_mask:0xf bank_mask:0xf
	v_add_f32_dpp v56, v56, v56 quad_perm:[2,3,0,1] row_mask:0xf bank_mask:0xf
	v_add_f32_dpp v57, v57, v57 quad_perm:[2,3,0,1] row_mask:0xf bank_mask:0xf
	v_sub_f32_e32 v60, v56, v55
	v_mul_f32_e32 v58, v57, v57
	v_cmp_gt_f32_e32 vcc, 0, v60
	v_mul_f32_e32 v59, v60, v60
	v_fmac_f32_e32 v59, 4.0, v58
	v_sqrt_f32_e32 v59, v59
	v_mul_f32_e32 v63, v62, v41
	v_mul_f32_e32 v43, v62, v40
	v_fma_f32 v40, v61, v40, -v63
	v_fma_f32 v41, v61, v41, v43
	v_add_f32_e64 v59, |v60|, v59
	v_add_f32_e32 v59, 0x0da24260, v59
	v_rcp_f32_e32 v59, v59
	v_add_f32_e32 v58, v57, v57
	v_mul_f32_e32 v59, v58, v59
	v_cndmask_b32_e64 v59, v59, -v59, vcc
	v_fma_f32 v58, v59, v59, 1.0
	v_rsq_f32_e32 v61, v58
	s_nop 0
	v_mul_f32_e32 v62, v61, v59
	v_mul_f32_e32 v55, v62, v54
	v_mul_f32_e32 v56, v62, v52
	v_fma_f32 v52, v61, v52, -v55
	v_fma_f32 v54, v61, v54, v56
	v_mul_f32_e32 v55, v53, v53
	v_mul_f32_e32 v56, v54, v54
	v_mul_f32_e32 v57, v53, v54
	v_add_f32_dpp v55, v55, v55 quad_perm:[1,0,3,2] row_mask:0xf bank_mask:0xf
	v_add_f32_dpp v56, v56, v56 quad_perm:[1,0,3,2] row_mask:0xf bank_mask:0xf
	v_add_f32_dpp v57, v57, v57 quad_perm:[1,0,3,2] row_mask:0xf bank_mask:0xf
	v_add_f32_dpp v55, v55, v55 quad_perm:[2,3,0,1] row_mask:0xf bank_mask:0xf
	v_add_f32_dpp v56, v56, v56 quad_perm:[2,3,0,1] row_mask:0xf bank_mask:0xf
	v_add_f32_dpp v57, v57, v57 quad_perm:[2,3,0,1] row_mask:0xf bank_mask:0xf
	v_sub_f32_e32 v60, v56, v55
	v_mul_f32_e32 v58, v57, v57
	v_cmp_gt_f32_e32 vcc, 0, v60
	v_mul_f32_e32 v59, v60, v60
	v_fmac_f32_e32 v59, 4.0, v58
	v_sqrt_f32_e32 v59, v59
	v_mul_f32_e32 v63, v62, v42
	v_mul_f32_e32 v43, v62, v40
	v_fma_f32 v40, v61, v40, -v63
	v_fma_f32 v42, v61, v42, v43
	v_add_f32_e64 v59, |v60|, v59
	v_add_f32_e32 v59, 0x0da24260, v59
	v_rcp_f32_e32 v59, v59
	v_add_f32_e32 v58, v57, v57
	v_mul_f32_e32 v59, v58, v59
	v_cndmask_b32_e64 v59, v59, -v59, vcc
	v_fma_f32 v58, v59, v59, 1.0
	v_rsq_f32_e32 v61, v58
	s_nop 0
	v_mul_f32_e32 v62, v61, v59
	v_mul_f32_e32 v55, v62, v54
	v_mul_f32_e32 v56, v62, v53
	v_fma_f32 v53, v61, v53, -v55
	v_fma_f32 v54, v61, v54, v56
	v_mul_f32_e32 v55, v52, v52
	v_mul_f32_e32 v56, v53, v53
	v_mul_f32_e32 v57, v52, v53
	v_add_f32_dpp v55, v55, v55 quad_perm:[1,0,3,2] row_mask:0xf bank_mask:0xf
	v_add_f32_dpp v56, v56, v56 quad_perm:[1,0,3,2] row_mask:0xf bank_mask:0xf
	v_add_f32_dpp v57, v57, v57 quad_perm:[1,0,3,2] row_mask:0xf bank_mask:0xf
	v_add_f32_dpp v55, v55, v55 quad_perm:[2,3,0,1] row_mask:0xf bank_mask:0xf
	v_add_f32_dpp v56, v56, v56 quad_perm:[2,3,0,1] row_mask:0xf bank_mask:0xf
	v_add_f32_dpp v57, v57, v57 quad_perm:[2,3,0,1] row_mask:0xf bank_mask:0xf
	v_sub_f32_e32 v60, v56, v55
	v_mul_f32_e32 v58, v57, v57
	v_cmp_gt_f32_e32 vcc, 0, v60
	v_mul_f32_e32 v59, v60, v60
	v_fmac_f32_e32 v59, 4.0, v58
	v_sqrt_f32_e32 v59, v59
	v_mul_f32_e32 v63, v62, v42
	v_mul_f32_e32 v43, v62, v41
	v_fma_f32 v41, v61, v41, -v63
	v_fma_f32 v42, v61, v42, v43
	v_add_f32_e64 v59, |v60|, v59
	v_add_f32_e32 v59, 0x0da24260, v59
	v_rcp_f32_e32 v59, v59
	v_add_f32_e32 v58, v57, v57
	v_mul_f32_e32 v59, v58, v59
	v_cndmask_b32_e64 v59, v59, -v59, vcc
	v_fma_f32 v58, v59, v59, 1.0
	v_rsq_f32_e32 v61, v58
	s_nop 0
	v_mul_f32_e32 v62, v61, v59
	v_mul_f32_e32 v55, v62, v53
	v_mul_f32_e32 v56, v62, v52
	v_fma_f32 v52, v61, v52, -v55
	v_fma_f32 v53, v61, v53, v56
	v_mul_f32_e32 v55, v52, v52
	v_mul_f32_e32 v56, v54, v54
	v_mul_f32_e32 v57, v52, v54
	v_add_f32_dpp v55, v55, v55 quad_perm:[1,0,3,2] row_mask:0xf bank_mask:0xf
	v_add_f32_dpp v56, v56, v56 quad_perm:[1,0,3,2] row_mask:0xf bank_mask:0xf
	v_add_f32_dpp v57, v57, v57 quad_perm:[1,0,3,2] row_mask:0xf bank_mask:0xf
	v_add_f32_dpp v55, v55, v55 quad_perm:[2,3,0,1] row_mask:0xf bank_mask:0xf
	v_add_f32_dpp v56, v56, v56 quad_perm:[2,3,0,1] row_mask:0xf bank_mask:0xf
	v_add_f32_dpp v57, v57, v57 quad_perm:[2,3,0,1] row_mask:0xf bank_mask:0xf
	v_sub_f32_e32 v60, v56, v55
	v_mul_f32_e32 v58, v57, v57
	v_cmp_gt_f32_e32 vcc, 0, v60
	v_mul_f32_e32 v59, v60, v60
	v_fmac_f32_e32 v59, 4.0, v58
	v_sqrt_f32_e32 v59, v59
	v_mul_f32_e32 v63, v62, v41
	v_mul_f32_e32 v43, v62, v40
	v_fma_f32 v40, v61, v40, -v63
	v_fma_f32 v41, v61, v41, v43
	v_add_f32_e64 v59, |v60|, v59
	v_add_f32_e32 v59, 0x0da24260, v59
	v_rcp_f32_e32 v59, v59
	v_add_f32_e32 v58, v57, v57
	v_mul_f32_e32 v59, v58, v59
	v_cndmask_b32_e64 v59, v59, -v59, vcc
	v_fma_f32 v58, v59, v59, 1.0
	v_rsq_f32_e32 v61, v58
	s_nop 0
	v_mul_f32_e32 v62, v61, v59
	v_mul_f32_e32 v55, v62, v54
	v_mul_f32_e32 v56, v62, v52
	v_fma_f32 v52, v61, v52, -v55
	v_fma_f32 v54, v61, v54, v56
	v_mul_f32_e32 v55, v53, v53
	v_mul_f32_e32 v56, v54, v54
	v_mul_f32_e32 v57, v53, v54
	v_add_f32_dpp v55, v55, v55 quad_perm:[1,0,3,2] row_mask:0xf bank_mask:0xf
	v_add_f32_dpp v56, v56, v56 quad_perm:[1,0,3,2] row_mask:0xf bank_mask:0xf
	v_add_f32_dpp v57, v57, v57 quad_perm:[1,0,3,2] row_mask:0xf bank_mask:0xf
	v_add_f32_dpp v55, v55, v55 quad_perm:[2,3,0,1] row_mask:0xf bank_mask:0xf
	v_add_f32_dpp v56, v56, v56 quad_perm:[2,3,0,1] row_mask:0xf bank_mask:0xf
	v_add_f32_dpp v57, v57, v57 quad_perm:[2,3,0,1] row_mask:0xf bank_mask:0xf
	v_sub_f32_e32 v60, v56, v55
	v_mul_f32_e32 v58, v57, v57
	v_cmp_gt_f32_e32 vcc, 0, v60
	v_mul_f32_e32 v59, v60, v60
	v_fmac_f32_e32 v59, 4.0, v58
	v_sqrt_f32_e32 v59, v59
	v_mul_f32_e32 v63, v62, v42
	v_mul_f32_e32 v43, v62, v40
	v_fma_f32 v40, v61, v40, -v63
	v_fma_f32 v42, v61, v42, v43
	v_add_f32_e64 v59, |v60|, v59
	v_add_f32_e32 v59, 0x0da24260, v59
	v_rcp_f32_e32 v59, v59
	v_add_f32_e32 v58, v57, v57
	v_mul_f32_e32 v59, v58, v59
	v_cndmask_b32_e64 v59, v59, -v59, vcc
	v_fma_f32 v58, v59, v59, 1.0
	v_rsq_f32_e32 v61, v58
	s_nop 0
	v_mul_f32_e32 v62, v61, v59
	v_mul_f32_e32 v55, v62, v54
	v_mul_f32_e32 v56, v62, v53
	v_fma_f32 v53, v61, v53, -v55
	v_fma_f32 v54, v61, v54, v56
	v_mul_f32_e32 v55, v52, v52
	v_mul_f32_e32 v56, v53, v53
	v_mul_f32_e32 v57, v52, v53
	v_add_f32_dpp v55, v55, v55 quad_perm:[1,0,3,2] row_mask:0xf bank_mask:0xf
	v_add_f32_dpp v56, v56, v56 quad_perm:[1,0,3,2] row_mask:0xf bank_mask:0xf
	v_add_f32_dpp v57, v57, v57 quad_perm:[1,0,3,2] row_mask:0xf bank_mask:0xf
	v_add_f32_dpp v55, v55, v55 quad_perm:[2,3,0,1] row_mask:0xf bank_mask:0xf
	v_add_f32_dpp v56, v56, v56 quad_perm:[2,3,0,1] row_mask:0xf bank_mask:0xf
	v_add_f32_dpp v57, v57, v57 quad_perm:[2,3,0,1] row_mask:0xf bank_mask:0xf
	v_sub_f32_e32 v60, v56, v55
	v_mul_f32_e32 v58, v57, v57
	v_cmp_gt_f32_e32 vcc, 0, v60
	v_mul_f32_e32 v59, v60, v60
	v_fmac_f32_e32 v59, 4.0, v58
	v_sqrt_f32_e32 v59, v59
	v_mul_f32_e32 v63, v62, v42
	v_mul_f32_e32 v43, v62, v41
	v_fma_f32 v41, v61, v41, -v63
	v_fma_f32 v42, v61, v42, v43
	v_add_f32_e64 v59, |v60|, v59
	v_add_f32_e32 v59, 0x0da24260, v59
	v_rcp_f32_e32 v59, v59
	v_add_f32_e32 v58, v57, v57
	v_mul_f32_e32 v59, v58, v59
	v_cndmask_b32_e64 v59, v59, -v59, vcc
	v_fma_f32 v58, v59, v59, 1.0
	v_rsq_f32_e32 v61, v58
	s_nop 0
	v_mul_f32_e32 v62, v61, v59
	v_mul_f32_e32 v55, v62, v53
	v_mul_f32_e32 v56, v62, v52
	v_fma_f32 v52, v61, v52, -v55
	v_fma_f32 v53, v61, v53, v56
	v_mul_f32_e32 v55, v52, v52
	v_mul_f32_e32 v56, v54, v54
	v_mul_f32_e32 v57, v52, v54
	v_add_f32_dpp v55, v55, v55 quad_perm:[1,0,3,2] row_mask:0xf bank_mask:0xf
	v_add_f32_dpp v56, v56, v56 quad_perm:[1,0,3,2] row_mask:0xf bank_mask:0xf
	v_add_f32_dpp v57, v57, v57 quad_perm:[1,0,3,2] row_mask:0xf bank_mask:0xf
	v_add_f32_dpp v55, v55, v55 quad_perm:[2,3,0,1] row_mask:0xf bank_mask:0xf
	v_add_f32_dpp v56, v56, v56 quad_perm:[2,3,0,1] row_mask:0xf bank_mask:0xf
	v_add_f32_dpp v57, v57, v57 quad_perm:[2,3,0,1] row_mask:0xf bank_mask:0xf
	v_sub_f32_e32 v60, v56, v55
	v_mul_f32_e32 v58, v57, v57
	v_cmp_gt_f32_e32 vcc, 0, v60
	v_mul_f32_e32 v59, v60, v60
	v_fmac_f32_e32 v59, 4.0, v58
	v_sqrt_f32_e32 v59, v59
	v_mul_f32_e32 v63, v62, v41
	v_mul_f32_e32 v43, v62, v40
	v_fma_f32 v40, v61, v40, -v63
	v_fma_f32 v41, v61, v41, v43
	v_add_f32_e64 v59, |v60|, v59
	v_add_f32_e32 v59, 0x0da24260, v59
	v_rcp_f32_e32 v59, v59
	v_add_f32_e32 v58, v57, v57
	v_mul_f32_e32 v59, v58, v59
	v_cndmask_b32_e64 v59, v59, -v59, vcc
	v_fma_f32 v58, v59, v59, 1.0
	v_rsq_f32_e32 v61, v58
	s_nop 0
	v_mul_f32_e32 v62, v61, v59
	v_mul_f32_e32 v55, v62, v54
	v_mul_f32_e32 v56, v62, v52
	v_fma_f32 v52, v61, v52, -v55
	v_fma_f32 v54, v61, v54, v56
	v_mul_f32_e32 v55, v53, v53
	v_mul_f32_e32 v56, v54, v54
	v_mul_f32_e32 v57, v53, v54
	v_add_f32_dpp v55, v55, v55 quad_perm:[1,0,3,2] row_mask:0xf bank_mask:0xf
	v_add_f32_dpp v56, v56, v56 quad_perm:[1,0,3,2] row_mask:0xf bank_mask:0xf
	v_add_f32_dpp v57, v57, v57 quad_perm:[1,0,3,2] row_mask:0xf bank_mask:0xf
	v_add_f32_dpp v55, v55, v55 quad_perm:[2,3,0,1] row_mask:0xf bank_mask:0xf
	v_add_f32_dpp v56, v56, v56 quad_perm:[2,3,0,1] row_mask:0xf bank_mask:0xf
	v_add_f32_dpp v57, v57, v57 quad_perm:[2,3,0,1] row_mask:0xf bank_mask:0xf
	v_sub_f32_e32 v60, v56, v55
	v_mul_f32_e32 v58, v57, v57
	v_cmp_gt_f32_e32 vcc, 0, v60
	v_mul_f32_e32 v59, v60, v60
	v_fmac_f32_e32 v59, 4.0, v58
	v_sqrt_f32_e32 v59, v59
	v_mul_f32_e32 v63, v62, v42
	v_mul_f32_e32 v43, v62, v40
	v_fma_f32 v40, v61, v40, -v63
	v_fma_f32 v42, v61, v42, v43
	v_add_f32_e64 v59, |v60|, v59
	v_add_f32_e32 v59, 0x0da24260, v59
	v_rcp_f32_e32 v59, v59
	v_add_f32_e32 v58, v57, v57
	v_mul_f32_e32 v59, v58, v59
	v_cndmask_b32_e64 v59, v59, -v59, vcc
	v_fma_f32 v58, v59, v59, 1.0
	v_rsq_f32_e32 v61, v58
	s_nop 0
	v_mul_f32_e32 v62, v61, v59
	v_mul_f32_e32 v55, v62, v54
	v_mul_f32_e32 v56, v62, v53
	v_fma_f32 v53, v61, v53, -v55
	v_fma_f32 v54, v61, v54, v56
	v_mul_f32_e32 v55, v52, v52
	v_mul_f32_e32 v56, v53, v53
	v_mul_f32_e32 v57, v52, v53
	v_add_f32_dpp v55, v55, v55 quad_perm:[1,0,3,2] row_mask:0xf bank_mask:0xf
	v_add_f32_dpp v56, v56, v56 quad_perm:[1,0,3,2] row_mask:0xf bank_mask:0xf
	v_add_f32_dpp v57, v57, v57 quad_perm:[1,0,3,2] row_mask:0xf bank_mask:0xf
	v_add_f32_dpp v55, v55, v55 quad_perm:[2,3,0,1] row_mask:0xf bank_mask:0xf
	v_add_f32_dpp v56, v56, v56 quad_perm:[2,3,0,1] row_mask:0xf bank_mask:0xf
	v_add_f32_dpp v57, v57, v57 quad_perm:[2,3,0,1] row_mask:0xf bank_mask:0xf
	v_sub_f32_e32 v60, v56, v55
	v_mul_f32_e32 v58, v57, v57
	v_cmp_gt_f32_e32 vcc, 0, v60
	v_mul_f32_e32 v59, v60, v60
	v_fmac_f32_e32 v59, 4.0, v58
	v_sqrt_f32_e32 v59, v59
	v_mul_f32_e32 v63, v62, v42
	v_mul_f32_e32 v43, v62, v41
	v_fma_f32 v41, v61, v41, -v63
	v_fma_f32 v42, v61, v42, v43
	v_add_f32_e64 v59, |v60|, v59
	v_add_f32_e32 v59, 0x0da24260, v59
	v_rcp_f32_e32 v59, v59
	v_add_f32_e32 v58, v57, v57
	v_mul_f32_e32 v59, v58, v59
	v_cndmask_b32_e64 v59, v59, -v59, vcc
	v_fma_f32 v58, v59, v59, 1.0
	v_rsq_f32_e32 v61, v58
	s_nop 0
	v_mul_f32_e32 v62, v61, v59
	v_mul_f32_e32 v55, v62, v53
	v_mul_f32_e32 v56, v62, v52
	v_fma_f32 v52, v61, v52, -v55
	v_fma_f32 v53, v61, v53, v56
	v_mul_f32_e32 v55, v52, v52
	v_mul_f32_e32 v56, v54, v54
	v_mul_f32_e32 v57, v52, v54
	v_add_f32_dpp v55, v55, v55 quad_perm:[1,0,3,2] row_mask:0xf bank_mask:0xf
	v_add_f32_dpp v56, v56, v56 quad_perm:[1,0,3,2] row_mask:0xf bank_mask:0xf
	v_add_f32_dpp v57, v57, v57 quad_perm:[1,0,3,2] row_mask:0xf bank_mask:0xf
	v_add_f32_dpp v55, v55, v55 quad_perm:[2,3,0,1] row_mask:0xf bank_mask:0xf
	v_add_f32_dpp v56, v56, v56 quad_perm:[2,3,0,1] row_mask:0xf bank_mask:0xf
	v_add_f32_dpp v57, v57, v57 quad_perm:[2,3,0,1] row_mask:0xf bank_mask:0xf
	v_sub_f32_e32 v60, v56, v55
	v_mul_f32_e32 v58, v57, v57
	v_cmp_gt_f32_e32 vcc, 0, v60
	v_mul_f32_e32 v59, v60, v60
	v_fmac_f32_e32 v59, 4.0, v58
	v_sqrt_f32_e32 v59, v59
	v_mul_f32_e32 v63, v62, v41
	v_mul_f32_e32 v43, v62, v40
	v_fma_f32 v40, v61, v40, -v63
	v_fma_f32 v41, v61, v41, v43
	v_add_f32_e64 v59, |v60|, v59
	v_add_f32_e32 v59, 0x0da24260, v59
	v_rcp_f32_e32 v59, v59
	v_add_f32_e32 v58, v57, v57
	v_mul_f32_e32 v59, v58, v59
	v_cndmask_b32_e64 v59, v59, -v59, vcc
	v_fma_f32 v58, v59, v59, 1.0
	v_rsq_f32_e32 v61, v58
	s_nop 0
	v_mul_f32_e32 v62, v61, v59
	v_mul_f32_e32 v55, v62, v54
	v_mul_f32_e32 v56, v62, v52
	v_fma_f32 v52, v61, v52, -v55
	v_fma_f32 v54, v61, v54, v56
	v_mul_f32_e32 v55, v53, v53
	v_mul_f32_e32 v56, v54, v54
	v_mul_f32_e32 v57, v53, v54
	v_add_f32_dpp v55, v55, v55 quad_perm:[1,0,3,2] row_mask:0xf bank_mask:0xf
	v_add_f32_dpp v56, v56, v56 quad_perm:[1,0,3,2] row_mask:0xf bank_mask:0xf
	v_add_f32_dpp v57, v57, v57 quad_perm:[1,0,3,2] row_mask:0xf bank_mask:0xf
	v_add_f32_dpp v55, v55, v55 quad_perm:[2,3,0,1] row_mask:0xf bank_mask:0xf
	v_add_f32_dpp v56, v56, v56 quad_perm:[2,3,0,1] row_mask:0xf bank_mask:0xf
	v_add_f32_dpp v57, v57, v57 quad_perm:[2,3,0,1] row_mask:0xf bank_mask:0xf
	v_sub_f32_e32 v60, v56, v55
	v_mul_f32_e32 v58, v57, v57
	v_cmp_gt_f32_e32 vcc, 0, v60
	v_mul_f32_e32 v59, v60, v60
	v_fmac_f32_e32 v59, 4.0, v58
	v_sqrt_f32_e32 v59, v59
	v_mul_f32_e32 v63, v62, v42
	v_mul_f32_e32 v43, v62, v40
	v_fma_f32 v40, v61, v40, -v63
	v_fma_f32 v42, v61, v42, v43
	v_add_f32_e64 v59, |v60|, v59
	v_add_f32_e32 v59, 0x0da24260, v59
	v_rcp_f32_e32 v59, v59
	v_add_f32_e32 v58, v57, v57
	v_mul_f32_e32 v59, v58, v59
	v_cndmask_b32_e64 v59, v59, -v59, vcc
	v_fma_f32 v58, v59, v59, 1.0
	v_rsq_f32_e32 v61, v58
	s_nop 0
	v_mul_f32_e32 v62, v61, v59
	v_mul_f32_e32 v55, v62, v54
	v_mul_f32_e32 v56, v62, v53
	v_fma_f32 v53, v61, v53, -v55
	v_fma_f32 v54, v61, v54, v56
	v_mul_f32_e32 v63, v62, v42
	v_mul_f32_e32 v43, v62, v41
	v_fma_f32 v41, v61, v41, -v63
	v_fma_f32 v42, v61, v42, v43
	v_mul_f32_e32 v55, v52, v52
	v_mul_f32_e32 v56, v53, v53
	v_mul_f32_e32 v57, v54, v54
	v_add_f32_dpp v55, v55, v55 quad_perm:[1,0,3,2] row_mask:0xf bank_mask:0xf
	v_add_f32_dpp v56, v56, v56 quad_perm:[1,0,3,2] row_mask:0xf bank_mask:0xf
	v_add_f32_dpp v57, v57, v57 quad_perm:[1,0,3,2] row_mask:0xf bank_mask:0xf
	v_add_f32_dpp v55, v55, v55 quad_perm:[2,3,0,1] row_mask:0xf bank_mask:0xf
	v_add_f32_dpp v56, v56, v56 quad_perm:[2,3,0,1] row_mask:0xf bank_mask:0xf
	v_add_f32_dpp v57, v57, v57 quad_perm:[2,3,0,1] row_mask:0xf bank_mask:0xf
	v_cmp_le_f32_e64 s[28:29], v55, v56
	v_cmp_le_f32_e64 s[30:31], v55, v57
	v_cmp_lt_f32_e32 vcc, v57, v56
	s_and_b64 s[28:29], s[28:29], s[30:31]
	s_andn2_b64 s[30:31], vcc, s[28:29]
	v_cndmask_b32_e64 v44, v52, v53, s[28:29]
	v_cndmask_b32_e64 v45, v54, v53, s[30:31]
	v_cndmask_b32_e64 v46, v40, v41, s[28:29]
	v_cndmask_b32_e64 v47, v42, v41, s[30:31]
	v_mul_f32_e32 v58, v44, v44
	s_nop 1
	v_add_f32_dpp v58, v58, v58 quad_perm:[1,0,3,2] row_mask:0xf bank_mask:0xf
	s_nop 1
	v_add_f32_dpp v58, v58, v58 quad_perm:[2,3,0,1] row_mask:0xf bank_mask:0xf
	v_max_f32_e32 v58, 0x3aa2425, v58
	v_rsq_f32_e32 v58, v58
	s_nop 0
	v_mul_f32_e32 v48, v44, v58
	v_mul_f32_e32 v59, v48, v45
	s_nop 1
	v_add_f32_dpp v59, v59, v59 quad_perm:[1,0,3,2] row_mask:0xf bank_mask:0xf
	s_nop 1
	v_add_f32_dpp v59, v59, v59 quad_perm:[2,3,0,1] row_mask:0xf bank_mask:0xf
	v_fma_f32 v49, -v59, v48, v45
	v_mul_f32_e32 v58, v49, v49
	s_nop 1
	v_add_f32_dpp v58, v58, v58 quad_perm:[1,0,3,2] row_mask:0xf bank_mask:0xf
	s_nop 1
	v_add_f32_dpp v58, v58, v58 quad_perm:[2,3,0,1] row_mask:0xf bank_mask:0xf
	v_max_f32_e32 v58, 0x3aa2425, v58
	v_rsq_f32_e32 v58, v58
	s_nop 0
	v_mul_f32_e32 v50, v49, v58
	v_mov_b32_dpp v43, v47 quad_perm:[2,0,1,3] row_mask:0xf bank_mask:0xf
	v_mov_b32_dpp v63, v47 quad_perm:[1,2,0,3] row_mask:0xf bank_mask:0xf
	v_mov_b32_dpp v62, v50 quad_perm:[2,0,1,3] row_mask:0xf bank_mask:0xf
	v_mov_b32_dpp v61, v50 quad_perm:[1,2,0,3] row_mask:0xf bank_mask:0xf
	v_mul_f32_dpp v60, v46, v43 quad_perm:[1,2,0,3] row_mask:0xf bank_mask:0xf
	v_mul_f32_dpp v51, v48, v62 quad_perm:[1,2,0,3] row_mask:0xf bank_mask:0xf
	s_nop 0
	v_fmac_f32_dpp v60, -v46, v63 quad_perm:[2,0,1,3] row_mask:0xf bank_mask:0xf
	v_fmac_f32_dpp v51, -v48, v61 quad_perm:[2,0,1,3] row_mask:0xf bank_mask:0xf
	v_mul_f32_dpp v52, v46, v48 quad_perm:[0,0,0,0] row_mask:0xf bank_mask:0xf
	v_mul_f32_dpp v53, v46, v48 quad_perm:[1,1,1,1] row_mask:0xf bank_mask:0xf
	v_mul_f32_dpp v54, v46, v48 quad_perm:[2,2,2,2] row_mask:0xf bank_mask:0xf
	v_fmac_f32_dpp v52, v47, v50 quad_perm:[0,0,0,0] row_mask:0xf bank_mask:0xf
	v_fmac_f32_dpp v53, v47, v50 quad_perm:[1,1,1,1] row_mask:0xf bank_mask:0xf
	v_fmac_f32_dpp v54, v47, v50 quad_perm:[2,2,2,2] row_mask:0xf bank_mask:0xf
	v_fmac_f32_dpp v52, v60, v51 quad_perm:[0,0,0,0] row_mask:0xf bank_mask:0xf
	v_fmac_f32_dpp v53, v60, v51 quad_perm:[1,1,1,1] row_mask:0xf bank_mask:0xf
	v_fmac_f32_dpp v54, v60, v51 quad_perm:[2,2,2,2] row_mask:0xf bank_mask:0xf
	v_mov_b32_e32 v55, 0
	v_writelane_b32 v55, s32, 48
	v_writelane_b32 v55, s33, 49
	v_writelane_b32 v55, s34, 50
	v_mul_f32_e32 v55, 0xbc800000, v55
	v_mul_f32_e32 v56, v55, v52
	v_mul_f32_e32 v57, v55, v53
	v_mul_f32_e32 v58, v55, v54
	v_add_f32_dpp v56, v56, v56 quad_perm:[1,0,3,2] row_mask:0xf bank_mask:0xf
	v_add_f32_dpp v57, v57, v57 quad_perm:[1,0,3,2] row_mask:0xf bank_mask:0xf
	v_add_f32_dpp v58, v58, v58 quad_perm:[1,0,3,2] row_mask:0xf bank_mask:0xf
	v_add_f32_dpp v56, v56, v56 quad_perm:[2,3,0,1] row_mask:0xf bank_mask:0xf
	v_add_f32_dpp v57, v57, v57 quad_perm:[2,3,0,1] row_mask:0xf bank_mask:0xf
	v_add_f32_dpp v58, v58, v58 quad_perm:[2,3,0,1] row_mask:0xf bank_mask:0xf
	v_cndmask_b32_e64 v52, v52, v56, s[26:27]
	v_cndmask_b32_e64 v53, v53, v57, s[26:27]
	v_cndmask_b32_e64 v54, v54, v58, s[26:27]
	v_subrev_u32_e32 v59, 48, v0
	v_lshlrev_b32_e32 v59, 4, v59
	s_mov_b32 s20, 0
	s_mov_b32 s21, 0xf0000
	s_mov_b64 exec, s[20:21]
	ds_write_b96 v59, v[52:54] offset:24576
	s_mov_b64 exec, -1
	s_waitcnt lgkmcnt(0)
	s_branch .Ljoin

.Ljoin:
	s_barrier
	v_mov_b32_e32 v6, 0x6000
	ds_read_b96 v[32:34], v6
	ds_read_b96 v[36:38], v6 offset:16
	ds_read_b96 v[40:42], v6 offset:32
	ds_read_b96 v[44:46], v6 offset:48
	v_add_u32_e32 v56, 0xc00, v3
	v_add_u32_e32 v57, 0x1200, v3
	ds_read2_b32 v[8:9], v3 offset0:0 offset1:1
	ds_read_b32 v24, v3 offset:8
	ds_read2_b32 v[10:11], v3 offset0:192 offset1:193
	ds_read_b32 v25, v3 offset:776
	ds_read2_b32 v[12:13], v4 offset0:0 offset1:1
	ds_read_b32 v26, v4 offset:8
	s_waitcnt lgkmcnt(4)
	v_fma_f32 v60, v8, v32, v44
	v_fma_f32 v61, v8, v33, v45
	v_fma_f32 v62, v8, v34, v46
	v_fmac_f32_e32 v60, v9, v36
	v_fmac_f32_e32 v61, v9, v37
	v_fmac_f32_e32 v62, v9, v38
	v_fmac_f32_e32 v60, v24, v40
	v_fmac_f32_e32 v61, v24, v41
	v_fmac_f32_e32 v62, v24, v42
	ds_write2_b32 v3, v60, v61 offset0:0 offset1:1
	ds_write_b32 v3, v62 offset:8
	ds_read2_b32 v[14:15], v4 offset0:192 offset1:193
	ds_read_b32 v27, v4 offset:776
	s_waitcnt lgkmcnt(6)
	v_fma_f32 v35, v10, v32, v44
	v_fma_f32 v39, v10, v33, v45
	v_fma_f32 v43, v10, v34, v46
	v_fmac_f32_e32 v35, v11, v36
	v_fmac_f32_e32 v39, v11, v37
	v_fmac_f32_e32 v43, v11, v38
	v_fmac_f32_e32 v35, v25, v40
	v_fmac_f32_e32 v39, v25, v41
	v_fmac_f32_e32 v43, v25, v42
	ds_write2_b32 v3, v35, v39 offset0:192 offset1:193
	ds_write_b32 v3, v43 offset:776
	ds_read2_b32 v[16:17], v56 offset0:0 offset1:1
	ds_read_b32 v28, v56 offset:8
	s_waitcnt lgkmcnt(8)
	v_fma_f32 v60, v12, v32, v44
	v_fma_f32 v61, v12, v33, v45
	v_fma_f32 v62, v12, v34, v46
	v_fmac_f32_e32 v60, v13, v36
	v_fmac_f32_e32 v61, v13, v37
	v_fmac_f32_e32 v62, v13, v38
	v_fmac_f32_e32 v60, v26, v40
	v_fmac_f32_e32 v61, v26, v41
	v_fmac_f32_e32 v62, v26, v42
	ds_write2_b32 v4, v60, v61 offset0:0 offset1:1
	ds_write_b32 v4, v62 offset:8
	ds_read2_b32 v[18:19], v56 offset0:192 offset1:193
	ds_read_b32 v29, v56 offset:776
	s_waitcnt lgkmcnt(8)
	v_fma_f32 v35, v14, v32, v44
	v_fma_f32 v39, v14, v33, v45
	v_fma_f32 v43, v14, v34, v46
	v_fmac_f32_e32 v35, v15, v36
	v_fmac_f32_e32 v39, v15, v37
	v_fmac_f32_e32 v43, v15, v38
	v_fmac_f32_e32 v35, v27, v40
	v_fmac_f32_e32 v39, v27, v41
	v_fmac_f32_e32 v43, v27, v42
	ds_write2_b32 v4, v35, v39 offset0:192 offset1:193
	ds_write_b32 v4, v43 offset:776
	ds_read2_b32 v[20:21], v57 offset0:0 offset1:1
	ds_read_b32 v30, v57 offset:8
	s_waitcnt lgkmcnt(8)
	v_fma_f32 v60, v16, v32, v44
	v_fma_f32 v61, v16, v33, v45
	v_fma_f32 v62, v16, v34, v46
	v_fmac_f32_e32 v60, v17, v36
	v_fmac_f32_e32 v61, v17, v37
	v_fmac_f32_e32 v62, v17, v38
	v_fmac_f32_e32 v60, v28, v40
	v_fmac_f32_e32 v61, v28, v41
	v_fmac_f32_e32 v62, v28, v42
	ds_write2_b32 v56, v60, v61 offset0:0 offset1:1
	ds_write_b32 v56, v62 offset:8
	ds_read2_b32 v[22:23], v57 offset0:192 offset1:193
	ds_read_b32 v31, v57 offset:776
	s_waitcnt lgkmcnt(8)
	v_fma_f32 v35, v18, v32, v44
	v_fma_f32 v39, v18, v33, v45
	v_fma_f32 v43, v18, v34, v46
	v_fmac_f32_e32 v35, v19, v36
	v_fmac_f32_e32 v39, v19, v37
	v_fmac_f32_e32 v43, v19, v38
	v_fmac_f32_e32 v35, v29, v40
	v_fmac_f32_e32 v39, v29, v41
	v_fmac_f32_e32 v43, v29, v42
	ds_write2_b32 v56, v35, v39 offset0:192 offset1:193
	ds_write_b32 v56, v43 offset:776
	s_waitcnt lgkmcnt(6)
	v_fma_f32 v60, v20, v32, v44
	v_fma_f32 v61, v20, v33, v45
	v_fma_f32 v62, v20, v34, v46
	v_fmac_f32_e32 v60, v21, v36
	v_fmac_f32_e32 v61, v21, v37
	v_fmac_f32_e32 v62, v21, v38
	v_fmac_f32_e32 v60, v30, v40
	v_fmac_f32_e32 v61, v30, v41
	v_fmac_f32_e32 v62, v30, v42
	ds_write2_b32 v57, v60, v61 offset0:0 offset1:1
	ds_write_b32 v57, v62 offset:8
	s_waitcnt lgkmcnt(4)
	v_fma_f32 v35, v22, v32, v44
	v_fma_f32 v39, v22, v33, v45
	v_fma_f32 v43, v22, v34, v46
	v_fmac_f32_e32 v35, v23, v36
	v_fmac_f32_e32 v39, v23, v37
	v_fmac_f32_e32 v43, v23, v38
	v_fmac_f32_e32 v35, v31, v40
	v_fmac_f32_e32 v39, v31, v41
	v_fmac_f32_e32 v43, v31, v42
	ds_write2_b32 v57, v35, v39 offset0:192 offset1:193
	ds_write_b32 v57, v43 offset:776
	ds_read_b128 v[8:11], v2
	ds_read_b128 v[12:15], v2 offset:1024
	ds_read_b128 v[16:19], v2 offset:2048
	ds_read_b128 v[20:23], v2 offset:3072
	ds_read_b128 v[24:27], v2 offset:4096
	ds_read_b128 v[28:31], v2 offset:5120
	s_waitcnt lgkmcnt(5)
	global_store_dwordx4 v1, v[8:11], s[10:11] offset:-2048 nt
	s_waitcnt lgkmcnt(4)
	global_store_dwordx4 v1, v[12:15], s[10:11] offset:-1024 nt
	s_waitcnt lgkmcnt(3)
	global_store_dwordx4 v1, v[16:19], s[10:11] offset:0 nt
	s_waitcnt lgkmcnt(2)
	global_store_dwordx4 v1, v[20:23], s[10:11] offset:1024 nt
	s_waitcnt lgkmcnt(1)
	global_store_dwordx4 v1, v[24:27], s[10:11] offset:2048 nt
	s_waitcnt lgkmcnt(0)
	s_and_saveexec_b64 s[16:17], s[14:15]
	global_store_dwordx4 v1, v[28:31], s[10:11] offset:3072 nt
	s_endpgm
